# v41 + MLA up-proj epilogue: rsq row loads batched 4 rows at a time, rope table row loaded once per iteration, token-pair rsq loads fetched two groups at a time
# speedup vs baseline: 1.0128x; 1.0021x over previous
.LBB6_773:
	s_lshl_b32 s0, s12, 8
	s_cmp_lg_u32 s84, 2
	s_mov_b64 s[4:5], -1
	v_add_u32_e32 v166, s0, v157
	s_cbranch_scc0 .LBB6_840
	s_cmp_lg_u32 s84, 0
	s_cselect_b64 s[4:5], -1, 0
	s_cmp_eq_u32 s84, 0
	s_mov_b32 s0, 0x7200000
	s_cselect_b32 s0, s0, 0x7e00000
	s_add_u32 s6, s8, s0
	s_addc_u32 s7, s9, 0
	v_ashrrev_i32_e32 v167, 31, v166
	s_cmp_lg_u32 s28, 2
	v_lshlrev_b64 v[132:133], 6, v[166:167]
	s_cselect_b64 s[30:31], -1, 0
	v_lshl_add_u64 v[132:133], s[2:3], 0, v[132:133]
	s_lshl_b64 s[34:35], s[84:85], 5
	v_lshl_add_u64 v[136:137], v[132:133], 0, s[34:35]
	flat_load_dwordx4 v[132:135], v[136:137]
	flat_load_dwordx4 v[236:239], v[136:137] offset:1024
	flat_load_dwordx4 v[240:243], v[136:137] offset:1040
	flat_load_dwordx4 v[244:247], v[136:137] offset:2048
	flat_load_dwordx4 v[248:251], v[136:137] offset:2064
	flat_load_dwordx4 v[228:231], v[136:137] offset:3072
	flat_load_dwordx4 v[232:235], v[136:137] offset:3088
	s_nop 0
	flat_load_dwordx4 v[136:139], v[136:137] offset:16
	s_or_b64 s[36:37], s[4:5], s[30:31]
	s_mov_b64 s[4:5], -1
	s_mul_i32 s30, s28, 0x180
	s_waitcnt vmcnt(0) lgkmcnt(0)
	v_mov_b32_e32 v140, v132
	v_mov_b32_e32 v141, v136
	v_mov_b32_e32 v136, v133
	v_pk_add_f32 v[132:133], v[140:141], v[136:137]
	v_mov_b32_e32 v136, v134
	v_mov_b32_e32 v137, v138
	v_mov_b32_e32 v138, v135
	v_pk_add_f32 v[134:135], v[136:137], v[138:139]
	s_nop 0
	v_pk_add_f32 v[132:133], v[132:133], v[134:135]
	s_nop 0
	v_add_f32_e32 v2, v132, v133
	v_fmamk_f32 v2, v2, 0x3b000000, v212
	v_cmp_gt_f32_e32 vcc, s58, v2
	v_mul_f32_e32 v132, 0x4b800000, v2
	s_nop 0
	v_cndmask_b32_e32 v2, v2, v132, vcc
	v_rsq_f32_e32 v2, v2
	s_nop 0
	v_mul_f32_e32 v132, 0x45800000, v2
	v_cndmask_b32_e32 v136, v2, v132, vcc
	v_mov_b64_e32 v[132:133], s[6:7]
	v_mad_i64_i32 v[134:135], s[0:1], v166, s70, v[132:133]
	v_lshlrev_b32_e32 v2, 1, v156
	v_lshl_add_u64 v[138:139], v[134:135], 0, v[2:3]
	v_pk_mul_f32 v[142:143], v[130:131], v[136:137] op_sel_hi:[1,0]
	v_pk_mul_f32 v[144:145], v[128:129], v[136:137] op_sel_hi:[1,0]
	v_pk_mul_f32 v[146:147], v[126:127], v[136:137] op_sel_hi:[1,0]
	v_pk_mul_f32 v[168:169], v[124:125], v[136:137] op_sel_hi:[1,0]
	s_and_b64 vcc, exec, s[36:37]
	s_cbranch_vccz .LBB6_776
	s_ashr_i32 s31, s30, 31
	v_cvt_pk_bf16_f32 v170, v144, v145
	v_cvt_pk_bf16_f32 v171, v142, v143
	v_cvt_pk_bf16_f32 v172, v168, v169
	v_cvt_pk_bf16_f32 v173, v146, v147
	v_lshl_add_u64 v[132:133], s[30:31], 1, v[138:139]
	flat_store_dwordx4 v[132:133], v[170:173]
	s_mov_b64 s[4:5], 0
.LBB6_776:
	v_lshlrev_b32_e32 v132, 5, v166
	v_and_b32_e32 v132, 0xf9e0, v132
	s_andn2_b64 vcc, exec, s[4:5]
	v_lshlrev_b32_e32 v140, 3, v132
	v_lshlrev_b32_e32 v132, 1, v158
	s_cbranch_vccnz .LBB6_778
	v_mov_b32_e32 v141, v3
	v_lshl_add_u64 v[174:175], v[160:161], 0, v[140:141]
	flat_load_dwordx4 v[170:173], v[174:175]
	s_nop 0
	flat_load_dwordx4 v[174:177], v[174:175] offset:16
	s_lshl_b32 s84, s68, 1
	v_mov_b32_e32 v133, v3
	s_waitcnt vmcnt(0) lgkmcnt(0)
	v_mov_b64_e32 v[202:203], v[170:171]
	v_mov_b64_e32 v[204:205], v[172:173]
	v_mov_b64_e32 v[206:207], v[174:175]
	v_mov_b64_e32 v[208:209], v[176:177]
	v_mov_b32_e32 v178, v171
	v_mov_b32_e32 v179, v173
	v_mov_b32_e32 v186, v175
	v_mov_b32_e32 v187, v177
	v_mov_b32_e32 v175, v176
	v_mov_b32_e32 v171, v172
	v_pk_mul_f32 v[184:185], v[168:169], v[178:179]
	v_pk_mul_f32 v[188:189], v[146:147], v[186:187]
	v_pk_mul_f32 v[168:169], v[168:169], v[170:171]
	v_pk_mul_f32 v[146:147], v[146:147], v[174:175]
	v_pk_fma_f32 v[176:177], v[142:143], v[174:175], v[188:189] neg_lo:[0,0,1] neg_hi:[0,0,1]
	v_pk_fma_f32 v[172:173], v[144:145], v[170:171], v[184:185] neg_lo:[0,0,1] neg_hi:[0,0,1]
	v_pk_fma_f32 v[142:143], v[142:143], v[186:187], v[146:147]
	v_pk_fma_f32 v[144:145], v[144:145], v[178:179], v[168:169]
	v_lshl_add_u64 v[146:147], v[134:135], 0, s[84:85]
	v_lshl_add_u64 v[146:147], v[146:147], 0, v[132:133]
	v_cvt_pk_bf16_f32 v168, v172, v173
	v_cvt_pk_bf16_f32 v169, v176, v177
	v_cvt_pk_bf16_f32 v144, v144, v145
	v_cvt_pk_bf16_f32 v145, v142, v143
	flat_store_dwordx2 v[146:147], v[168:169] offset:256
	flat_store_dwordx2 v[146:147], v[144:145] offset:320

.LBB6_780:
	s_andn2_b64 vcc, exec, s[36:37]
	s_cbranch_vccnz .LBB6_782
	v_mov_b32_e32 v141, v3
	v_lshl_add_u64 v[168:169], v[160:161], 0, v[140:141]
	v_mov_b64_e32 v[138:139], v[202:203]
	v_mov_b64_e32 v[140:141], v[204:205]
	s_nop 0
	v_mov_b64_e32 v[168:169], v[206:207]
	v_mov_b64_e32 v[170:171], v[208:209]
	s_lshl_b32 s84, s68, 1
	v_mov_b32_e32 v133, v3
	v_lshl_add_u64 v[134:135], v[134:135], 0, s[84:85]
	v_lshl_add_u64 v[134:135], v[134:135], 0, v[132:133]
	v_mov_b32_e32 v172, v139
	v_mov_b32_e32 v173, v141
	v_mov_b32_e32 v174, v169
	v_mov_b32_e32 v175, v171
	v_mov_b32_e32 v169, v170
	v_mov_b32_e32 v139, v140
	v_pk_mul_f32 v[140:141], v[136:137], v[172:173]
	v_pk_mul_f32 v[170:171], v[146:147], v[174:175]
	v_pk_mul_f32 v[136:137], v[136:137], v[138:139]
	v_pk_mul_f32 v[146:147], v[146:147], v[168:169]
	v_pk_fma_f32 v[168:169], v[142:143], v[168:169], v[170:171] neg_lo:[0,0,1] neg_hi:[0,0,1]
	v_pk_fma_f32 v[138:139], v[144:145], v[138:139], v[140:141] neg_lo:[0,0,1] neg_hi:[0,0,1]
	v_pk_fma_f32 v[140:141], v[142:143], v[174:175], v[146:147]
	v_pk_fma_f32 v[136:137], v[144:145], v[172:173], v[136:137]
	v_cvt_pk_bf16_f32 v138, v138, v139
	v_cvt_pk_bf16_f32 v139, v168, v169
	v_cvt_pk_bf16_f32 v136, v136, v137
	v_cvt_pk_bf16_f32 v137, v140, v141
	flat_store_dwordx2 v[134:135], v[138:139] offset:1024
	flat_store_dwordx2 v[134:135], v[136:137] offset:1088
.LBB6_782:
	v_or_b32_e32 v140, 16, v166
	v_ashrrev_i32_e32 v141, 31, v140
	v_lshlrev_b64 v[134:135], 6, v[140:141]
	v_lshl_add_u64 v[134:135], s[2:3], 0, v[134:135]
	v_lshl_add_u64 v[138:139], v[134:135], 0, s[34:35]
	v_mov_b64_e32 v[134:135], v[236:237]
	v_mov_b64_e32 v[136:137], v[238:239]
	v_mov_b64_e32 v[142:143], v[240:241]
	v_mov_b64_e32 v[144:145], v[242:243]
	s_mov_b64 s[36:37], -1
	v_mov_b32_e32 v138, v134
	v_mov_b32_e32 v139, v142
	v_mov_b32_e32 v142, v135
	v_pk_add_f32 v[134:135], v[138:139], v[142:143]
	v_mov_b32_e32 v138, v136
	v_mov_b32_e32 v139, v144
	v_mov_b32_e32 v144, v137
	v_pk_add_f32 v[136:137], v[138:139], v[144:145]
	s_nop 0
	v_pk_add_f32 v[134:135], v[134:135], v[136:137]
	v_mov_b64_e32 v[136:137], s[6:7]
	v_add_f32_e32 v133, v134, v135
	v_fmamk_f32 v133, v133, 0x3b000000, v212
	v_cmp_gt_f32_e32 vcc, s58, v133
	v_mul_f32_e32 v134, 0x4b800000, v133
	v_mad_i64_i32 v[136:137], s[0:1], v140, s70, v[136:137]
	v_cndmask_b32_e32 v133, v133, v134, vcc
	v_rsq_f32_e32 v133, v133
	v_lshl_add_u64 v[138:139], v[136:137], 0, v[2:3]
	v_mul_f32_e32 v134, 0x45800000, v133
	v_cndmask_b32_e32 v134, v133, v134, vcc
	v_pk_mul_f32 v[142:143], v[122:123], v[134:135] op_sel_hi:[1,0]
	v_pk_mul_f32 v[144:145], v[120:121], v[134:135] op_sel_hi:[1,0]
	v_pk_mul_f32 v[146:147], v[118:119], v[134:135] op_sel_hi:[1,0]
	v_pk_mul_f32 v[168:169], v[116:117], v[134:135] op_sel_hi:[1,0]
	s_and_b64 vcc, exec, s[4:5]
	s_cbranch_vccnz .LBB6_784
	s_ashr_i32 s31, s30, 31
	v_cvt_pk_bf16_f32 v170, v144, v145
	v_cvt_pk_bf16_f32 v171, v142, v143
	v_cvt_pk_bf16_f32 v172, v168, v169
	v_cvt_pk_bf16_f32 v173, v146, v147
	v_lshl_add_u64 v[174:175], s[30:31], 1, v[138:139]
	s_mov_b64 s[36:37], 0
	flat_store_dwordx4 v[174:175], v[170:173]
.LBB6_784:
	v_lshlrev_b32_e32 v133, 5, v140
	v_and_b32_e32 v133, 0xfbe0, v133
	s_andn2_b64 vcc, exec, s[36:37]
	v_lshlrev_b32_e32 v140, 3, v133
	s_cbranch_vccnz .LBB6_786
	v_mov_b32_e32 v141, v3
	v_lshl_add_u64 v[174:175], v[160:161], 0, v[140:141]
	flat_load_dwordx4 v[170:173], v[174:175]
	s_nop 0
	flat_load_dwordx4 v[174:177], v[174:175] offset:16
	s_lshl_b32 s84, s68, 1
	v_mov_b32_e32 v133, v3
	s_waitcnt vmcnt(0) lgkmcnt(0)
	v_mov_b64_e32 v[202:203], v[170:171]
	v_mov_b64_e32 v[204:205], v[172:173]
	v_mov_b64_e32 v[206:207], v[174:175]
	v_mov_b64_e32 v[208:209], v[176:177]
	v_mov_b32_e32 v178, v171
	v_mov_b32_e32 v179, v173
	v_mov_b32_e32 v186, v175
	v_mov_b32_e32 v187, v177
	v_mov_b32_e32 v175, v176
	v_mov_b32_e32 v171, v172
	v_pk_mul_f32 v[184:185], v[168:169], v[178:179]
	v_pk_mul_f32 v[188:189], v[146:147], v[186:187]
	v_pk_mul_f32 v[168:169], v[168:169], v[170:171]
	v_pk_mul_f32 v[146:147], v[146:147], v[174:175]
	v_pk_fma_f32 v[176:177], v[142:143], v[174:175], v[188:189] neg_lo:[0,0,1] neg_hi:[0,0,1]
	v_pk_fma_f32 v[172:173], v[144:145], v[170:171], v[184:185] neg_lo:[0,0,1] neg_hi:[0,0,1]
	v_pk_fma_f32 v[142:143], v[142:143], v[186:187], v[146:147]
	v_pk_fma_f32 v[144:145], v[144:145], v[178:179], v[168:169]
	v_lshl_add_u64 v[146:147], v[136:137], 0, s[84:85]
	v_lshl_add_u64 v[146:147], v[146:147], 0, v[132:133]
	v_cvt_pk_bf16_f32 v168, v172, v173
	v_cvt_pk_bf16_f32 v169, v176, v177
	v_cvt_pk_bf16_f32 v144, v144, v145
	v_cvt_pk_bf16_f32 v145, v142, v143
	flat_store_dwordx2 v[146:147], v[168:169] offset:256
	flat_store_dwordx2 v[146:147], v[144:145] offset:320

.LBB6_788:
	s_andn2_b64 vcc, exec, s[36:37]
	s_cbranch_vccnz .LBB6_790
	v_mov_b32_e32 v141, v3
	v_lshl_add_u64 v[168:169], v[160:161], 0, v[140:141]
	v_mov_b64_e32 v[138:139], v[202:203]
	v_mov_b64_e32 v[140:141], v[204:205]
	s_nop 0
	v_mov_b64_e32 v[168:169], v[206:207]
	v_mov_b64_e32 v[170:171], v[208:209]
	s_lshl_b32 s84, s68, 1
	v_mov_b32_e32 v133, v3
	v_lshl_add_u64 v[136:137], v[136:137], 0, s[84:85]
	v_lshl_add_u64 v[136:137], v[136:137], 0, v[132:133]
	v_mov_b32_e32 v172, v139
	v_mov_b32_e32 v173, v141
	v_mov_b32_e32 v174, v169
	v_mov_b32_e32 v175, v171
	v_mov_b32_e32 v169, v170
	v_mov_b32_e32 v139, v140
	v_pk_mul_f32 v[140:141], v[134:135], v[172:173]
	v_pk_mul_f32 v[170:171], v[146:147], v[174:175]
	v_pk_mul_f32 v[134:135], v[134:135], v[138:139]
	v_pk_mul_f32 v[146:147], v[146:147], v[168:169]
	v_pk_fma_f32 v[168:169], v[142:143], v[168:169], v[170:171] neg_lo:[0,0,1] neg_hi:[0,0,1]
	v_pk_fma_f32 v[138:139], v[144:145], v[138:139], v[140:141] neg_lo:[0,0,1] neg_hi:[0,0,1]
	v_pk_fma_f32 v[140:141], v[142:143], v[174:175], v[146:147]
	v_pk_fma_f32 v[134:135], v[144:145], v[172:173], v[134:135]
	v_cvt_pk_bf16_f32 v138, v138, v139
	v_cvt_pk_bf16_f32 v139, v168, v169
	v_cvt_pk_bf16_f32 v134, v134, v135
	v_cvt_pk_bf16_f32 v135, v140, v141
	flat_store_dwordx2 v[136:137], v[138:139] offset:1024
	flat_store_dwordx2 v[136:137], v[134:135] offset:1088
.LBB6_790:
	v_or_b32_e32 v140, 32, v166
	v_ashrrev_i32_e32 v141, 31, v140
	v_lshlrev_b64 v[134:135], 6, v[140:141]
	v_lshl_add_u64 v[134:135], s[2:3], 0, v[134:135]
	v_lshl_add_u64 v[138:139], v[134:135], 0, s[34:35]
	v_mov_b64_e32 v[134:135], v[244:245]
	v_mov_b64_e32 v[136:137], v[246:247]
	v_mov_b64_e32 v[142:143], v[248:249]
	v_mov_b64_e32 v[144:145], v[250:251]
	s_mov_b64 s[36:37], -1
	v_mov_b32_e32 v138, v134
	v_mov_b32_e32 v139, v142
	v_mov_b32_e32 v142, v135
	v_pk_add_f32 v[134:135], v[138:139], v[142:143]
	v_mov_b32_e32 v138, v136
	v_mov_b32_e32 v139, v144
	v_mov_b32_e32 v144, v137
	v_pk_add_f32 v[136:137], v[138:139], v[144:145]
	s_nop 0
	v_pk_add_f32 v[134:135], v[134:135], v[136:137]
	v_mov_b64_e32 v[136:137], s[6:7]
	v_add_f32_e32 v133, v134, v135
	v_fmamk_f32 v133, v133, 0x3b000000, v212
	v_cmp_gt_f32_e32 vcc, s58, v133
	v_mul_f32_e32 v134, 0x4b800000, v133
	v_mad_i64_i32 v[136:137], s[0:1], v140, s70, v[136:137]
	v_cndmask_b32_e32 v133, v133, v134, vcc
	v_rsq_f32_e32 v133, v133
	v_lshl_add_u64 v[138:139], v[136:137], 0, v[2:3]
	v_mul_f32_e32 v134, 0x45800000, v133
	v_cndmask_b32_e32 v134, v133, v134, vcc
	v_pk_mul_f32 v[142:143], v[114:115], v[134:135] op_sel_hi:[1,0]
	v_pk_mul_f32 v[144:145], v[112:113], v[134:135] op_sel_hi:[1,0]
	v_pk_mul_f32 v[146:147], v[110:111], v[134:135] op_sel_hi:[1,0]
	v_pk_mul_f32 v[168:169], v[108:109], v[134:135] op_sel_hi:[1,0]
	s_and_b64 vcc, exec, s[4:5]
	s_cbranch_vccnz .LBB6_792
	s_ashr_i32 s31, s30, 31
	v_cvt_pk_bf16_f32 v170, v144, v145
	v_cvt_pk_bf16_f32 v171, v142, v143
	v_cvt_pk_bf16_f32 v172, v168, v169
	v_cvt_pk_bf16_f32 v173, v146, v147
	v_lshl_add_u64 v[174:175], s[30:31], 1, v[138:139]
	s_mov_b64 s[36:37], 0
	flat_store_dwordx4 v[174:175], v[170:173]
.LBB6_792:
	v_lshlrev_b32_e32 v133, 5, v140
	v_and_b32_e32 v133, 0xfde0, v133
	s_andn2_b64 vcc, exec, s[36:37]
	v_lshlrev_b32_e32 v140, 3, v133
	s_cbranch_vccnz .LBB6_794
	v_mov_b32_e32 v141, v3
	v_lshl_add_u64 v[174:175], v[160:161], 0, v[140:141]
	flat_load_dwordx4 v[170:173], v[174:175]
	s_nop 0
	flat_load_dwordx4 v[174:177], v[174:175] offset:16
	s_lshl_b32 s84, s68, 1
	v_mov_b32_e32 v133, v3
	s_waitcnt vmcnt(0) lgkmcnt(0)
	v_mov_b64_e32 v[202:203], v[170:171]
	v_mov_b64_e32 v[204:205], v[172:173]
	v_mov_b64_e32 v[206:207], v[174:175]
	v_mov_b64_e32 v[208:209], v[176:177]
	v_mov_b32_e32 v178, v171
	v_mov_b32_e32 v179, v173
	v_mov_b32_e32 v186, v175
	v_mov_b32_e32 v187, v177
	v_mov_b32_e32 v175, v176
	v_mov_b32_e32 v171, v172
	v_pk_mul_f32 v[184:185], v[168:169], v[178:179]
	v_pk_mul_f32 v[188:189], v[146:147], v[186:187]
	v_pk_mul_f32 v[168:169], v[168:169], v[170:171]
	v_pk_mul_f32 v[146:147], v[146:147], v[174:175]
	v_pk_fma_f32 v[176:177], v[142:143], v[174:175], v[188:189] neg_lo:[0,0,1] neg_hi:[0,0,1]
	v_pk_fma_f32 v[172:173], v[144:145], v[170:171], v[184:185] neg_lo:[0,0,1] neg_hi:[0,0,1]
	v_pk_fma_f32 v[142:143], v[142:143], v[186:187], v[146:147]
	v_pk_fma_f32 v[144:145], v[144:145], v[178:179], v[168:169]
	v_lshl_add_u64 v[146:147], v[136:137], 0, s[84:85]
	v_lshl_add_u64 v[146:147], v[146:147], 0, v[132:133]
	v_cvt_pk_bf16_f32 v168, v172, v173
	v_cvt_pk_bf16_f32 v169, v176, v177
	v_cvt_pk_bf16_f32 v144, v144, v145
	v_cvt_pk_bf16_f32 v145, v142, v143
	flat_store_dwordx2 v[146:147], v[168:169] offset:256
	flat_store_dwordx2 v[146:147], v[144:145] offset:320

.LBB6_798:
	v_or_b32_e32 v140, 48, v166
	v_ashrrev_i32_e32 v141, 31, v140
	v_lshlrev_b64 v[134:135], 6, v[140:141]
	v_lshl_add_u64 v[134:135], s[2:3], 0, v[134:135]
	v_lshl_add_u64 v[138:139], v[134:135], 0, s[34:35]
	v_mov_b64_e32 v[134:135], v[228:229]
	v_mov_b64_e32 v[136:137], v[230:231]
	v_mov_b64_e32 v[142:143], v[232:233]
	v_mov_b64_e32 v[144:145], v[234:235]
	s_mov_b64 s[36:37], -1
	v_mov_b32_e32 v138, v134
	v_mov_b32_e32 v139, v142
	v_mov_b32_e32 v142, v135
	v_pk_add_f32 v[134:135], v[138:139], v[142:143]
	v_mov_b32_e32 v138, v136
	v_mov_b32_e32 v139, v144
	v_mov_b32_e32 v144, v137
	v_pk_add_f32 v[136:137], v[138:139], v[144:145]
	s_nop 0
	v_pk_add_f32 v[134:135], v[134:135], v[136:137]
	v_mov_b64_e32 v[136:137], s[6:7]
	v_add_f32_e32 v133, v134, v135
	v_fmamk_f32 v133, v133, 0x3b000000, v212
	v_cmp_gt_f32_e32 vcc, s58, v133
	v_mul_f32_e32 v134, 0x4b800000, v133
	v_mad_i64_i32 v[136:137], s[0:1], v140, s70, v[136:137]
	v_cndmask_b32_e32 v133, v133, v134, vcc
	v_rsq_f32_e32 v133, v133
	v_lshl_add_u64 v[138:139], v[136:137], 0, v[2:3]
	v_mul_f32_e32 v134, 0x45800000, v133
	v_cndmask_b32_e32 v134, v133, v134, vcc
	v_pk_mul_f32 v[142:143], v[106:107], v[134:135] op_sel_hi:[1,0]
	v_pk_mul_f32 v[144:145], v[104:105], v[134:135] op_sel_hi:[1,0]
	v_pk_mul_f32 v[146:147], v[102:103], v[134:135] op_sel_hi:[1,0]
	v_pk_mul_f32 v[168:169], v[100:101], v[134:135] op_sel_hi:[1,0]
	s_and_b64 vcc, exec, s[4:5]
	s_cbranch_vccnz .LBB6_800
	s_ashr_i32 s31, s30, 31
	v_cvt_pk_bf16_f32 v170, v144, v145
	v_cvt_pk_bf16_f32 v171, v142, v143
	v_cvt_pk_bf16_f32 v172, v168, v169
	v_cvt_pk_bf16_f32 v173, v146, v147
	v_lshl_add_u64 v[174:175], s[30:31], 1, v[138:139]
	s_mov_b64 s[36:37], 0
	flat_store_dwordx4 v[174:175], v[170:173]
.LBB6_800:
	v_lshlrev_b32_e32 v133, 5, v140
	v_and_b32_e32 v133, 0xffe0, v133
	s_andn2_b64 vcc, exec, s[36:37]
	v_lshlrev_b32_e32 v140, 3, v133
	s_cbranch_vccnz .LBB6_802
	v_mov_b32_e32 v141, v3
	v_lshl_add_u64 v[174:175], v[160:161], 0, v[140:141]
	flat_load_dwordx4 v[170:173], v[174:175]
	s_nop 0
	flat_load_dwordx4 v[174:177], v[174:175] offset:16
	s_lshl_b32 s84, s68, 1
	v_mov_b32_e32 v133, v3
	s_waitcnt vmcnt(0) lgkmcnt(0)
	v_mov_b64_e32 v[202:203], v[170:171]
	v_mov_b64_e32 v[204:205], v[172:173]
	v_mov_b64_e32 v[206:207], v[174:175]
	v_mov_b64_e32 v[208:209], v[176:177]
	v_mov_b32_e32 v178, v171
	v_mov_b32_e32 v179, v173
	v_mov_b32_e32 v186, v175
	v_mov_b32_e32 v187, v177
	v_mov_b32_e32 v175, v176
	v_mov_b32_e32 v171, v172
	v_pk_mul_f32 v[184:185], v[168:169], v[178:179]
	v_pk_mul_f32 v[188:189], v[146:147], v[186:187]
	v_pk_mul_f32 v[168:169], v[168:169], v[170:171]
	v_pk_mul_f32 v[146:147], v[146:147], v[174:175]
	v_pk_fma_f32 v[176:177], v[142:143], v[174:175], v[188:189] neg_lo:[0,0,1] neg_hi:[0,0,1]
	v_pk_fma_f32 v[172:173], v[144:145], v[170:171], v[184:185] neg_lo:[0,0,1] neg_hi:[0,0,1]
	v_pk_fma_f32 v[142:143], v[142:143], v[186:187], v[146:147]
	v_pk_fma_f32 v[144:145], v[144:145], v[178:179], v[168:169]
	v_lshl_add_u64 v[146:147], v[136:137], 0, s[84:85]
	v_lshl_add_u64 v[146:147], v[146:147], 0, v[132:133]
	v_cvt_pk_bf16_f32 v168, v172, v173
	v_cvt_pk_bf16_f32 v169, v176, v177
	v_cvt_pk_bf16_f32 v144, v144, v145
	v_cvt_pk_bf16_f32 v145, v142, v143
	flat_store_dwordx2 v[146:147], v[168:169] offset:256
	flat_store_dwordx2 v[146:147], v[144:145] offset:320

.LBB6_806:
	v_add_u32_e32 v140, 0x80, v166
	v_ashrrev_i32_e32 v141, 31, v140
	v_lshlrev_b64 v[134:135], 6, v[140:141]
	v_lshl_add_u64 v[134:135], s[2:3], 0, v[134:135]
	v_lshl_add_u64 v[138:139], v[134:135], 0, s[34:35]
	flat_load_dwordx4 v[134:137], v[138:139]
	flat_load_dwordx4 v[142:145], v[138:139] offset:16
	flat_load_dwordx4 v[236:239], v[138:139] offset:1024
	flat_load_dwordx4 v[240:243], v[138:139] offset:1040
	flat_load_dwordx4 v[244:247], v[138:139] offset:2048
	flat_load_dwordx4 v[248:251], v[138:139] offset:2064
	flat_load_dwordx4 v[228:231], v[138:139] offset:3072
	flat_load_dwordx4 v[232:235], v[138:139] offset:3088
	s_mov_b64 s[36:37], -1
	s_waitcnt vmcnt(0) lgkmcnt(0)
	v_mov_b32_e32 v138, v134
	v_mov_b32_e32 v139, v142
	v_mov_b32_e32 v142, v135
	v_pk_add_f32 v[134:135], v[138:139], v[142:143]
	v_mov_b32_e32 v138, v136
	v_mov_b32_e32 v139, v144
	v_mov_b32_e32 v144, v137
	v_pk_add_f32 v[136:137], v[138:139], v[144:145]
	s_nop 0
	v_pk_add_f32 v[134:135], v[134:135], v[136:137]
	v_mov_b64_e32 v[136:137], s[6:7]
	v_add_f32_e32 v133, v134, v135
	v_fmamk_f32 v133, v133, 0x3b000000, v212
	v_cmp_gt_f32_e32 vcc, s58, v133
	v_mul_f32_e32 v134, 0x4b800000, v133
	v_mad_i64_i32 v[136:137], s[0:1], v140, s70, v[136:137]
	v_cndmask_b32_e32 v133, v133, v134, vcc
	v_rsq_f32_e32 v133, v133
	v_lshl_add_u64 v[138:139], v[136:137], 0, v[2:3]
	v_mul_f32_e32 v134, 0x45800000, v133
	v_cndmask_b32_e32 v134, v133, v134, vcc
	v_pk_mul_f32 v[142:143], v[98:99], v[134:135] op_sel_hi:[1,0]
	v_pk_mul_f32 v[144:145], v[96:97], v[134:135] op_sel_hi:[1,0]
	v_pk_mul_f32 v[146:147], v[94:95], v[134:135] op_sel_hi:[1,0]
	v_pk_mul_f32 v[168:169], v[92:93], v[134:135] op_sel_hi:[1,0]
	s_and_b64 vcc, exec, s[4:5]
	s_cbranch_vccnz .LBB6_808
	s_ashr_i32 s31, s30, 31
	v_cvt_pk_bf16_f32 v170, v144, v145
	v_cvt_pk_bf16_f32 v171, v142, v143
	v_cvt_pk_bf16_f32 v172, v168, v169
	v_cvt_pk_bf16_f32 v173, v146, v147
	v_lshl_add_u64 v[174:175], s[30:31], 1, v[138:139]
	s_mov_b64 s[36:37], 0
	flat_store_dwordx4 v[174:175], v[170:173]
.LBB6_808:
	v_lshlrev_b32_e32 v133, 5, v140
	v_and_b32_e32 v133, 0xf9e0, v133
	s_andn2_b64 vcc, exec, s[36:37]
	v_lshlrev_b32_e32 v140, 3, v133
	s_cbranch_vccnz .LBB6_810
	v_mov_b32_e32 v141, v3
	v_lshl_add_u64 v[174:175], v[160:161], 0, v[140:141]
	flat_load_dwordx4 v[170:173], v[174:175]
	s_nop 0
	flat_load_dwordx4 v[174:177], v[174:175] offset:16
	s_lshl_b32 s84, s68, 1
	v_mov_b32_e32 v133, v3
	s_waitcnt vmcnt(0) lgkmcnt(0)
	v_mov_b64_e32 v[202:203], v[170:171]
	v_mov_b64_e32 v[204:205], v[172:173]
	v_mov_b64_e32 v[206:207], v[174:175]
	v_mov_b64_e32 v[208:209], v[176:177]
	v_mov_b32_e32 v178, v171
	v_mov_b32_e32 v179, v173
	v_mov_b32_e32 v186, v175
	v_mov_b32_e32 v187, v177
	v_mov_b32_e32 v175, v176
	v_mov_b32_e32 v171, v172
	v_pk_mul_f32 v[184:185], v[168:169], v[178:179]
	v_pk_mul_f32 v[188:189], v[146:147], v[186:187]
	v_pk_mul_f32 v[168:169], v[168:169], v[170:171]
	v_pk_mul_f32 v[146:147], v[146:147], v[174:175]
	v_pk_fma_f32 v[176:177], v[142:143], v[174:175], v[188:189] neg_lo:[0,0,1] neg_hi:[0,0,1]
	v_pk_fma_f32 v[172:173], v[144:145], v[170:171], v[184:185] neg_lo:[0,0,1] neg_hi:[0,0,1]
	v_pk_fma_f32 v[142:143], v[142:143], v[186:187], v[146:147]
	v_pk_fma_f32 v[144:145], v[144:145], v[178:179], v[168:169]
	v_lshl_add_u64 v[146:147], v[136:137], 0, s[84:85]
	v_lshl_add_u64 v[146:147], v[146:147], 0, v[132:133]
	v_cvt_pk_bf16_f32 v168, v172, v173
	v_cvt_pk_bf16_f32 v169, v176, v177
	v_cvt_pk_bf16_f32 v144, v144, v145
	v_cvt_pk_bf16_f32 v145, v142, v143
	flat_store_dwordx2 v[146:147], v[168:169] offset:256
	flat_store_dwordx2 v[146:147], v[144:145] offset:320

.LBB6_814:
	v_add_u32_e32 v140, 0x90, v166
	v_ashrrev_i32_e32 v141, 31, v140
	v_lshlrev_b64 v[134:135], 6, v[140:141]
	v_lshl_add_u64 v[134:135], s[2:3], 0, v[134:135]
	v_lshl_add_u64 v[138:139], v[134:135], 0, s[34:35]
	v_mov_b64_e32 v[134:135], v[236:237]
	v_mov_b64_e32 v[136:137], v[238:239]
	v_mov_b64_e32 v[142:143], v[240:241]
	v_mov_b64_e32 v[144:145], v[242:243]
	s_mov_b64 s[36:37], -1
	v_mov_b32_e32 v138, v134
	v_mov_b32_e32 v139, v142
	v_mov_b32_e32 v142, v135
	v_pk_add_f32 v[134:135], v[138:139], v[142:143]
	v_mov_b32_e32 v138, v136
	v_mov_b32_e32 v139, v144
	v_mov_b32_e32 v144, v137
	v_pk_add_f32 v[136:137], v[138:139], v[144:145]
	s_nop 0
	v_pk_add_f32 v[134:135], v[134:135], v[136:137]
	v_mov_b64_e32 v[136:137], s[6:7]
	v_add_f32_e32 v133, v134, v135
	v_fmamk_f32 v133, v133, 0x3b000000, v212
	v_cmp_gt_f32_e32 vcc, s58, v133
	v_mul_f32_e32 v134, 0x4b800000, v133
	v_mad_i64_i32 v[136:137], s[0:1], v140, s70, v[136:137]
	v_cndmask_b32_e32 v133, v133, v134, vcc
	v_rsq_f32_e32 v133, v133
	v_lshl_add_u64 v[138:139], v[136:137], 0, v[2:3]
	v_mul_f32_e32 v134, 0x45800000, v133
	v_cndmask_b32_e32 v134, v133, v134, vcc
	v_pk_mul_f32 v[142:143], v[90:91], v[134:135] op_sel_hi:[1,0]
	v_pk_mul_f32 v[144:145], v[88:89], v[134:135] op_sel_hi:[1,0]
	v_pk_mul_f32 v[146:147], v[86:87], v[134:135] op_sel_hi:[1,0]
	v_pk_mul_f32 v[168:169], v[84:85], v[134:135] op_sel_hi:[1,0]
	s_and_b64 vcc, exec, s[4:5]
	s_cbranch_vccnz .LBB6_816
	s_ashr_i32 s31, s30, 31
	v_cvt_pk_bf16_f32 v170, v144, v145
	v_cvt_pk_bf16_f32 v171, v142, v143
	v_cvt_pk_bf16_f32 v172, v168, v169
	v_cvt_pk_bf16_f32 v173, v146, v147
	v_lshl_add_u64 v[174:175], s[30:31], 1, v[138:139]
	s_mov_b64 s[36:37], 0
	flat_store_dwordx4 v[174:175], v[170:173]

.LBB6_822:
	v_add_u32_e32 v140, 0xa0, v166
	v_ashrrev_i32_e32 v141, 31, v140
	v_lshlrev_b64 v[134:135], 6, v[140:141]
	v_lshl_add_u64 v[134:135], s[2:3], 0, v[134:135]
	v_lshl_add_u64 v[138:139], v[134:135], 0, s[34:35]
	v_mov_b64_e32 v[134:135], v[244:245]
	v_mov_b64_e32 v[136:137], v[246:247]
	v_mov_b64_e32 v[142:143], v[248:249]
	v_mov_b64_e32 v[144:145], v[250:251]
	s_mov_b64 s[36:37], -1
	v_mov_b32_e32 v138, v134
	v_mov_b32_e32 v139, v142
	v_mov_b32_e32 v142, v135
	v_pk_add_f32 v[134:135], v[138:139], v[142:143]
	v_mov_b32_e32 v138, v136
	v_mov_b32_e32 v139, v144
	v_mov_b32_e32 v144, v137
	v_pk_add_f32 v[136:137], v[138:139], v[144:145]
	s_nop 0
	v_pk_add_f32 v[134:135], v[134:135], v[136:137]
	v_mov_b64_e32 v[136:137], s[6:7]
	v_add_f32_e32 v133, v134, v135
	v_fmamk_f32 v133, v133, 0x3b000000, v212
	v_cmp_gt_f32_e32 vcc, s58, v133
	v_mul_f32_e32 v134, 0x4b800000, v133
	v_mad_i64_i32 v[136:137], s[0:1], v140, s70, v[136:137]
	v_cndmask_b32_e32 v133, v133, v134, vcc
	v_rsq_f32_e32 v133, v133
	v_lshl_add_u64 v[138:139], v[136:137], 0, v[2:3]
	v_mul_f32_e32 v134, 0x45800000, v133
	v_cndmask_b32_e32 v134, v133, v134, vcc
	v_pk_mul_f32 v[142:143], v[82:83], v[134:135] op_sel_hi:[1,0]
	v_pk_mul_f32 v[144:145], v[80:81], v[134:135] op_sel_hi:[1,0]
	v_pk_mul_f32 v[146:147], v[78:79], v[134:135] op_sel_hi:[1,0]
	v_pk_mul_f32 v[168:169], v[76:77], v[134:135] op_sel_hi:[1,0]
	s_and_b64 vcc, exec, s[4:5]
	s_cbranch_vccnz .LBB6_824
	s_ashr_i32 s31, s30, 31
	v_cvt_pk_bf16_f32 v170, v144, v145
	v_cvt_pk_bf16_f32 v171, v142, v143
	v_cvt_pk_bf16_f32 v172, v168, v169
	v_cvt_pk_bf16_f32 v173, v146, v147
	v_lshl_add_u64 v[174:175], s[30:31], 1, v[138:139]
	s_mov_b64 s[36:37], 0
	flat_store_dwordx4 v[174:175], v[170:173]

.LBB6_830:
	v_add_u32_e32 v140, 0xb0, v166
	v_ashrrev_i32_e32 v141, 31, v140
	v_lshlrev_b64 v[134:135], 6, v[140:141]
	v_lshl_add_u64 v[134:135], s[2:3], 0, v[134:135]
	v_lshl_add_u64 v[138:139], v[134:135], 0, s[34:35]
	v_mov_b64_e32 v[134:135], v[228:229]
	v_mov_b64_e32 v[136:137], v[230:231]
	v_mov_b64_e32 v[142:143], v[232:233]
	v_mov_b64_e32 v[144:145], v[234:235]
	v_mov_b64_e32 v[138:139], s[6:7]
	s_and_b64 vcc, exec, s[4:5]
	v_mov_b32_e32 v146, v134
	v_mov_b32_e32 v147, v142
	v_mov_b32_e32 v142, v135
	v_mov_b32_e32 v134, v136
	v_mov_b32_e32 v135, v144
	v_mov_b32_e32 v144, v137
	v_pk_add_f32 v[136:137], v[146:147], v[142:143]
	v_pk_add_f32 v[134:135], v[134:135], v[144:145]
	s_nop 0
	v_pk_add_f32 v[134:135], v[136:137], v[134:135]
	s_nop 0
	v_add_f32_e32 v133, v134, v135
	v_fmamk_f32 v133, v133, 0x3b000000, v212
	v_mul_f32_e32 v134, 0x4b800000, v133
	v_cmp_gt_f32_e64 s[6:7], s58, v133
	s_nop 1
	v_cndmask_b32_e64 v133, v133, v134, s[6:7]
	v_rsq_f32_e32 v133, v133
	v_mad_i64_i32 v[134:135], s[0:1], v140, s70, v[138:139]
	v_lshl_add_u64 v[136:137], v[134:135], 0, v[2:3]
	v_mul_f32_e32 v2, 0x45800000, v133
	v_cndmask_b32_e64 v138, v133, v2, s[6:7]
	v_pk_mul_f32 v[142:143], v[74:75], v[138:139] op_sel_hi:[1,0]
	v_pk_mul_f32 v[144:145], v[72:73], v[138:139] op_sel_hi:[1,0]
	v_pk_mul_f32 v[146:147], v[70:71], v[138:139] op_sel_hi:[1,0]
	v_pk_mul_f32 v[168:169], v[68:69], v[138:139] op_sel_hi:[1,0]
	s_mov_b64 s[6:7], -1
	s_cbranch_vccnz .LBB6_832
	s_ashr_i32 s31, s30, 31
	v_cvt_pk_bf16_f32 v170, v144, v145
	v_cvt_pk_bf16_f32 v171, v142, v143
	v_cvt_pk_bf16_f32 v172, v168, v169
	v_cvt_pk_bf16_f32 v173, v146, v147
	v_lshl_add_u64 v[174:175], s[30:31], 1, v[136:137]
	s_mov_b64 s[6:7], 0
	flat_store_dwordx4 v[174:175], v[170:173]
.LBB6_832:
	v_lshlrev_b32_e32 v2, 5, v140
	v_and_b32_e32 v2, 0xffe0, v2
	s_andn2_b64 vcc, exec, s[6:7]
	v_lshlrev_b32_e32 v2, 3, v2
	s_cbranch_vccnz .LBB6_834
	v_lshl_add_u64 v[140:141], v[160:161], 0, v[2:3]
	flat_load_dwordx4 v[170:173], v[140:141]
	flat_load_dwordx4 v[174:177], v[140:141] offset:16
	s_lshl_b32 s84, s68, 1
	v_mov_b32_e32 v133, v3
	s_waitcnt vmcnt(0) lgkmcnt(0)
	v_mov_b64_e32 v[202:203], v[170:171]
	v_mov_b64_e32 v[204:205], v[172:173]
	v_mov_b64_e32 v[206:207], v[174:175]
	v_mov_b64_e32 v[208:209], v[176:177]
	v_mov_b32_e32 v140, v171
	v_mov_b32_e32 v141, v173
	v_mov_b32_e32 v184, v175
	v_mov_b32_e32 v185, v177
	v_mov_b32_e32 v175, v176
	v_mov_b32_e32 v171, v172
	v_pk_mul_f32 v[178:179], v[168:169], v[140:141]
	v_pk_mul_f32 v[186:187], v[146:147], v[184:185]
	v_pk_mul_f32 v[168:169], v[168:169], v[170:171]
	v_pk_mul_f32 v[146:147], v[146:147], v[174:175]
	v_pk_fma_f32 v[176:177], v[142:143], v[174:175], v[186:187] neg_lo:[0,0,1] neg_hi:[0,0,1]
	v_pk_fma_f32 v[172:173], v[144:145], v[170:171], v[178:179] neg_lo:[0,0,1] neg_hi:[0,0,1]
	v_pk_fma_f32 v[142:143], v[142:143], v[184:185], v[146:147]
	v_pk_fma_f32 v[140:141], v[144:145], v[140:141], v[168:169]
	v_lshl_add_u64 v[144:145], v[134:135], 0, s[84:85]
	v_lshl_add_u64 v[144:145], v[144:145], 0, v[132:133]
	v_cvt_pk_bf16_f32 v146, v172, v173
	v_cvt_pk_bf16_f32 v147, v176, v177
	v_cvt_pk_bf16_f32 v140, v140, v141
	v_cvt_pk_bf16_f32 v141, v142, v143
	flat_store_dwordx2 v[144:145], v[146:147] offset:256
	flat_store_dwordx2 v[144:145], v[140:141] offset:320

.LBB6_836:
	s_andn2_b64 vcc, exec, s[4:5]
	s_cbranch_vccnz .LBB6_838
	v_lshl_add_u64 v[136:137], v[160:161], 0, v[2:3]
	v_mov_b64_e32 v[168:169], v[202:203]
	v_mov_b64_e32 v[170:171], v[204:205]
	v_mov_b64_e32 v[172:173], v[206:207]
	v_mov_b64_e32 v[174:175], v[208:209]
	s_lshl_b32 s84, s68, 1
	v_mov_b32_e32 v133, v3
	v_lshl_add_u64 v[134:135], v[134:135], 0, s[84:85]
	v_lshl_add_u64 v[132:133], v[134:135], 0, v[132:133]
	v_mov_b32_e32 v134, v169
	v_mov_b32_e32 v135, v171
	v_mov_b32_e32 v136, v173
	v_mov_b32_e32 v137, v175
	v_mov_b32_e32 v173, v174
	v_mov_b32_e32 v169, v170
	v_pk_mul_f32 v[146:147], v[138:139], v[134:135]
	v_pk_mul_f32 v[170:171], v[144:145], v[136:137]
	v_pk_mul_f32 v[138:139], v[138:139], v[168:169]
	v_pk_mul_f32 v[144:145], v[144:145], v[172:173]
	v_pk_fma_f32 v[170:171], v[140:141], v[172:173], v[170:171] neg_lo:[0,0,1] neg_hi:[0,0,1]
	v_pk_fma_f32 v[146:147], v[142:143], v[168:169], v[146:147] neg_lo:[0,0,1] neg_hi:[0,0,1]
	v_pk_fma_f32 v[136:137], v[140:141], v[136:137], v[144:145]
	v_pk_fma_f32 v[134:135], v[142:143], v[134:135], v[138:139]
	v_cvt_pk_bf16_f32 v138, v146, v147
	v_cvt_pk_bf16_f32 v139, v170, v171
	v_cvt_pk_bf16_f32 v134, v134, v135
	v_cvt_pk_bf16_f32 v135, v136, v137
	flat_store_dwordx2 v[132:133], v[138:139] offset:1024
	flat_store_dwordx2 v[132:133], v[134:135] offset:1088

.LBB6_840:
	s_and_b64 vcc, exec, s[4:5]
	s_cbranch_vccz .LBB6_839
	v_lshl_or_b32 v170, s28, 8, v156
	v_or_b32_e32 v140, 1, v170
	v_ashrrev_i32_e32 v171, 31, v170
	v_ashrrev_i32_e32 v141, 31, v140
	v_lshlrev_b64 v[132:133], 6, v[170:171]
	v_lshlrev_b64 v[140:141], 6, v[140:141]
	v_lshl_add_u64 v[136:137], s[2:3], 0, v[132:133]
	v_lshl_add_u64 v[144:145], s[2:3], 0, v[140:141]
	flat_load_dwordx4 v[132:135], v[136:137] offset:32
	flat_load_dwordx4 v[236:239], v[136:137] offset:160
	flat_load_dwordx4 v[240:243], v[136:137] offset:176
	flat_load_dwordx4 v[244:247], v[136:137] offset:224
	flat_load_dwordx4 v[248:251], v[136:137] offset:240
	s_nop 0
	flat_load_dwordx4 v[136:139], v[136:137] offset:48
	s_nop 0
	flat_load_dwordx4 v[140:143], v[144:145] offset:32
	s_nop 0
	flat_load_dwordx4 v[144:147], v[144:145] offset:48
	s_mov_b32 s0, 0x358637bd
	s_mov_b32 s6, 0x3b000000
	s_mov_b32 s12, 0x45800000
	v_lshl_add_u64 v[172:173], v[170:171], 1, s[16:17]
	s_waitcnt vmcnt(0) lgkmcnt(0)
	v_mov_b32_e32 v168, v132
	v_mov_b32_e32 v169, v140
	v_mov_b32_e32 v140, v133
	v_pk_add_f32 v[132:133], v[168:169], v[140:141]
	v_mov_b32_e32 v140, v134
	v_mov_b32_e32 v141, v142
	v_mov_b32_e32 v142, v135
	v_pk_add_f32 v[134:135], v[140:141], v[142:143]
	v_mov_b64_e32 v[168:169], s[0:1]
	v_pk_add_f32 v[132:133], v[132:133], v[134:135]
	v_mov_b32_e32 v134, v136
	v_mov_b32_e32 v135, v144
	v_mov_b32_e32 v144, v137
	v_mov_b32_e32 v136, v138
	v_mov_b32_e32 v137, v146
	v_mov_b32_e32 v146, v139
	v_pk_add_f32 v[134:135], v[134:135], v[144:145]
	v_pk_add_f32 v[136:137], v[136:137], v[146:147]
	v_or_b32_e32 v140, 3, v170
	v_pk_add_f32 v[134:135], v[134:135], v[136:137]
	v_ashrrev_i32_e32 v141, 31, v140
	v_pk_add_f32 v[132:133], v[132:133], v[134:135]
	v_lshlrev_b64 v[140:141], 6, v[140:141]
	v_pk_fma_f32 v[132:133], v[132:133], s[6:7], v[168:169] op_sel_hi:[1,0,0]
	v_lshl_add_u64 v[144:145], s[2:3], 0, v[140:141]
	v_mul_f32_e32 v2, 0x4b800000, v132
	v_cmp_gt_f32_e64 s[4:5], s58, v132
	v_cmp_gt_f32_e32 vcc, s58, v133
	s_nop 0
	v_cndmask_b32_e64 v2, v132, v2, s[4:5]
	v_rsq_f32_e32 v132, v2
	v_mul_f32_e32 v2, 0x4b800000, v133
	v_cndmask_b32_e32 v2, v133, v2, vcc
	v_rsq_f32_e32 v133, v2
	s_nop 0
	v_pk_mul_f32 v[134:135], v[132:133], s[12:13] op_sel_hi:[1,0]
	s_nop 0
	v_cndmask_b32_e64 v174, v132, v134, s[4:5]
	v_or_b32_e32 v132, 2, v170
	v_cndmask_b32_e32 v175, v133, v135, vcc
	v_ashrrev_i32_e32 v133, 31, v132
	v_lshlrev_b64 v[132:133], 6, v[132:133]
	v_lshl_add_u64 v[136:137], s[2:3], 0, v[132:133]
	v_mov_b64_e32 v[132:133], v[236:237]
	v_mov_b64_e32 v[134:135], v[238:239]
	s_nop 0
	v_mov_b64_e32 v[136:137], v[240:241]
	v_mov_b64_e32 v[138:139], v[242:243]
	s_nop 0
	v_mov_b64_e32 v[140:141], v[244:245]
	v_mov_b64_e32 v[142:143], v[246:247]
	s_nop 0
	v_mov_b64_e32 v[144:145], v[248:249]
	v_mov_b64_e32 v[146:147], v[250:251]
	v_pk_mul_f32 v[128:129], v[128:129], v[174:175]
	v_pk_mul_f32 v[120:121], v[120:121], v[174:175]
	v_pk_mul_f32 v[112:113], v[112:113], v[174:175]
	v_pk_mul_f32 v[104:105], v[104:105], v[174:175]
	v_pk_mul_f32 v[96:97], v[96:97], v[174:175]
	v_pk_mul_f32 v[88:89], v[88:89], v[174:175]
	v_pk_mul_f32 v[80:81], v[80:81], v[174:175]
	v_pk_mul_f32 v[72:73], v[72:73], v[174:175]
	v_mov_b32_e32 v176, v132
	v_mov_b32_e32 v177, v140
	v_mov_b32_e32 v140, v133
	v_pk_add_f32 v[132:133], v[176:177], v[140:141]
	v_mov_b32_e32 v140, v134
	v_mov_b32_e32 v141, v142
	v_mov_b32_e32 v142, v135
	v_pk_add_f32 v[134:135], v[140:141], v[142:143]
	v_or_b32_e32 v140, 5, v170
	v_pk_add_f32 v[132:133], v[132:133], v[134:135]
	v_mov_b32_e32 v134, v136
	v_mov_b32_e32 v135, v144
	v_mov_b32_e32 v144, v137
	v_mov_b32_e32 v136, v138
	v_mov_b32_e32 v137, v146
	v_mov_b32_e32 v146, v139
	v_pk_add_f32 v[134:135], v[134:135], v[144:145]
	v_pk_add_f32 v[136:137], v[136:137], v[146:147]
	v_ashrrev_i32_e32 v141, 31, v140
	v_pk_add_f32 v[134:135], v[134:135], v[136:137]
	v_lshlrev_b64 v[140:141], 6, v[140:141]
	v_pk_add_f32 v[132:133], v[132:133], v[134:135]
	v_lshl_add_u64 v[144:145], s[2:3], 0, v[140:141]
	v_pk_fma_f32 v[132:133], v[132:133], s[6:7], v[168:169] op_sel_hi:[1,0,0]
	s_nop 0
	v_mul_f32_e32 v2, 0x4b800000, v132
	v_cmp_gt_f32_e64 s[4:5], s58, v132
	v_cmp_gt_f32_e32 vcc, s58, v133
	s_nop 0
	v_cndmask_b32_e64 v2, v132, v2, s[4:5]
	v_rsq_f32_e32 v132, v2
	v_mul_f32_e32 v2, 0x4b800000, v133
	v_cndmask_b32_e32 v2, v133, v2, vcc
	v_rsq_f32_e32 v133, v2
	s_nop 0
	v_pk_mul_f32 v[134:135], v[132:133], s[12:13] op_sel_hi:[1,0]
	s_nop 0
	v_cndmask_b32_e64 v176, v132, v134, s[4:5]
	v_or_b32_e32 v132, 4, v170
	v_cndmask_b32_e32 v177, v133, v135, vcc
	v_ashrrev_i32_e32 v133, 31, v132
	v_lshlrev_b64 v[132:133], 6, v[132:133]
	v_lshl_add_u64 v[136:137], s[2:3], 0, v[132:133]
	flat_load_dwordx4 v[132:135], v[136:137] offset:32
	flat_load_dwordx4 v[236:239], v[136:137] offset:160
	flat_load_dwordx4 v[240:243], v[136:137] offset:176
	flat_load_dwordx4 v[244:247], v[136:137] offset:224
	flat_load_dwordx4 v[248:251], v[136:137] offset:240
	s_nop 0
	flat_load_dwordx4 v[136:139], v[136:137] offset:48
	s_nop 0
	flat_load_dwordx4 v[140:143], v[144:145] offset:32
	s_nop 0
	flat_load_dwordx4 v[144:147], v[144:145] offset:48
	v_pk_mul_f32 v[130:131], v[130:131], v[176:177]
	v_pk_mul_f32 v[122:123], v[122:123], v[176:177]
	v_pk_mul_f32 v[114:115], v[114:115], v[176:177]
	v_pk_mul_f32 v[106:107], v[106:107], v[176:177]
	v_pk_mul_f32 v[98:99], v[98:99], v[176:177]
	v_pk_mul_f32 v[90:91], v[90:91], v[176:177]
	v_pk_mul_f32 v[82:83], v[82:83], v[176:177]
	v_pk_mul_f32 v[74:75], v[74:75], v[176:177]
	s_waitcnt vmcnt(0) lgkmcnt(0)
	v_mov_b32_e32 v178, v132
	v_mov_b32_e32 v179, v140
	v_mov_b32_e32 v140, v133
	v_pk_add_f32 v[132:133], v[178:179], v[140:141]
	v_mov_b32_e32 v140, v134
	v_mov_b32_e32 v141, v142
	v_mov_b32_e32 v142, v135
	v_pk_add_f32 v[134:135], v[140:141], v[142:143]
	v_or_b32_e32 v140, 7, v170
	v_pk_add_f32 v[132:133], v[132:133], v[134:135]
	v_mov_b32_e32 v134, v136
	v_mov_b32_e32 v135, v144
	v_mov_b32_e32 v144, v137
	v_mov_b32_e32 v136, v138
	v_mov_b32_e32 v137, v146
	v_mov_b32_e32 v146, v139
	v_pk_add_f32 v[134:135], v[134:135], v[144:145]
	v_pk_add_f32 v[136:137], v[136:137], v[146:147]
	v_ashrrev_i32_e32 v141, 31, v140
	v_pk_add_f32 v[134:135], v[134:135], v[136:137]
	v_lshlrev_b64 v[140:141], 6, v[140:141]
	v_pk_add_f32 v[132:133], v[132:133], v[134:135]
	v_lshl_add_u64 v[140:141], s[2:3], 0, v[140:141]
	v_pk_fma_f32 v[132:133], v[132:133], s[6:7], v[168:169] op_sel_hi:[1,0,0]
	s_nop 0
	v_mul_f32_e32 v2, 0x4b800000, v132
	v_cmp_gt_f32_e64 s[4:5], s58, v132
	v_cmp_gt_f32_e32 vcc, s58, v133
	s_nop 0
	v_cndmask_b32_e64 v2, v132, v2, s[4:5]
	v_rsq_f32_e32 v132, v2
	v_mul_f32_e32 v2, 0x4b800000, v133
	v_cndmask_b32_e32 v2, v133, v2, vcc
	v_rsq_f32_e32 v133, v2
	s_nop 0
	v_pk_mul_f32 v[134:135], v[132:133], s[12:13] op_sel_hi:[1,0]
	s_nop 0
	v_cndmask_b32_e64 v178, v132, v134, s[4:5]
	v_or_b32_e32 v132, 6, v170
	v_cndmask_b32_e32 v179, v133, v135, vcc
	v_ashrrev_i32_e32 v133, 31, v132
	v_lshlrev_b64 v[132:133], 6, v[132:133]
	v_lshl_add_u64 v[132:133], s[2:3], 0, v[132:133]
	v_mov_b64_e32 v[136:137], v[236:237]
	v_mov_b64_e32 v[138:139], v[238:239]
	s_nop 0
	v_mov_b64_e32 v[132:133], v[240:241]
	v_mov_b64_e32 v[134:135], v[242:243]
	s_nop 0
	v_mov_b64_e32 v[144:145], v[244:245]
	v_mov_b64_e32 v[146:147], v[246:247]
	s_nop 0
	v_mov_b64_e32 v[140:141], v[248:249]
	v_mov_b64_e32 v[142:143], v[250:251]
	v_pk_mul_f32 v[124:125], v[124:125], v[178:179]
	v_pk_mul_f32 v[116:117], v[116:117], v[178:179]
	v_pk_mul_f32 v[108:109], v[108:109], v[178:179]
	v_pk_mul_f32 v[100:101], v[100:101], v[178:179]
	v_pk_mul_f32 v[92:93], v[92:93], v[178:179]
	v_pk_mul_f32 v[84:85], v[84:85], v[178:179]
	v_mov_b32_e32 v184, v136
	v_mov_b32_e32 v185, v144
	v_mov_b32_e32 v144, v137
	v_pk_add_f32 v[136:137], v[184:185], v[144:145]
	v_mov_b32_e32 v144, v138
	v_mov_b32_e32 v145, v146
	v_mov_b32_e32 v146, v139
	v_pk_add_f32 v[138:139], v[144:145], v[146:147]
	s_nop 0
	v_pk_add_f32 v[136:137], v[136:137], v[138:139]
	v_mov_b32_e32 v138, v132
	v_mov_b32_e32 v139, v140
	v_mov_b32_e32 v140, v133
	v_pk_add_f32 v[132:133], v[138:139], v[140:141]
	v_mov_b32_e32 v138, v134
	v_mov_b32_e32 v139, v142
	v_mov_b32_e32 v142, v135
	v_pk_add_f32 v[134:135], v[138:139], v[142:143]
	s_nop 0
	v_pk_add_f32 v[132:133], v[132:133], v[134:135]
	s_nop 0
	v_pk_add_f32 v[132:133], v[136:137], v[132:133]
	s_nop 0
	v_pk_fma_f32 v[132:133], v[132:133], s[6:7], v[168:169] op_sel_hi:[1,0,0]
	s_nop 0
	v_mul_f32_e32 v2, 0x4b800000, v132
	v_cmp_gt_f32_e64 s[4:5], s58, v132
	v_cmp_gt_f32_e32 vcc, s58, v133
	s_nop 0
	v_cndmask_b32_e64 v2, v132, v2, s[4:5]
	v_rsq_f32_e32 v132, v2
	v_mul_f32_e32 v2, 0x4b800000, v133
	v_cndmask_b32_e32 v2, v133, v2, vcc
	v_rsq_f32_e32 v133, v2
	v_or_b32_e32 v2, 16, v166
	v_pk_mul_f32 v[134:135], v[132:133], s[12:13] op_sel_hi:[1,0]
	s_nop 0
	v_cndmask_b32_e32 v133, v133, v135, vcc
	v_cndmask_b32_e64 v132, v132, v134, s[4:5]
	v_pk_mul_f32 v[134:135], v[126:127], v[132:133]
	v_cvt_pk_bf16_f32 v126, v128, v129
	v_cvt_pk_bf16_f32 v127, v130, v131
	v_cvt_pk_bf16_f32 v128, v124, v125
	v_cvt_pk_bf16_f32 v129, v134, v135
	v_mad_i64_i32 v[124:125], s[0:1], v166, s55, v[172:173]
	flat_store_dwordx4 v[124:125], v[126:129]
	s_nop 1
	v_pk_mul_f32 v[126:127], v[118:119], v[132:133]
	v_cvt_pk_bf16_f32 v118, v120, v121
	v_cvt_pk_bf16_f32 v119, v122, v123
	v_cvt_pk_bf16_f32 v120, v116, v117
	v_cvt_pk_bf16_f32 v121, v126, v127
	v_mad_i64_i32 v[116:117], s[0:1], v2, s55, v[172:173]
	flat_store_dwordx4 v[116:117], v[118:121]
	v_or_b32_e32 v2, 32, v166
	s_nop 0
	v_pk_mul_f32 v[118:119], v[110:111], v[132:133]
	v_cvt_pk_bf16_f32 v110, v112, v113
	v_cvt_pk_bf16_f32 v111, v114, v115
	v_cvt_pk_bf16_f32 v112, v108, v109
	v_cvt_pk_bf16_f32 v113, v118, v119
	v_mad_i64_i32 v[108:109], s[0:1], v2, s55, v[172:173]
	flat_store_dwordx4 v[108:109], v[110:113]
	v_or_b32_e32 v2, 48, v166
	s_nop 0
	v_pk_mul_f32 v[110:111], v[102:103], v[132:133]
	v_cvt_pk_bf16_f32 v102, v104, v105
	v_cvt_pk_bf16_f32 v103, v106, v107
	v_cvt_pk_bf16_f32 v104, v100, v101
	v_cvt_pk_bf16_f32 v105, v110, v111
	v_mad_i64_i32 v[100:101], s[0:1], v2, s55, v[172:173]
	flat_store_dwordx4 v[100:101], v[102:105]
	v_add_u32_e32 v2, 0x80, v166
	s_nop 0
	v_pk_mul_f32 v[102:103], v[94:95], v[132:133]
	v_cvt_pk_bf16_f32 v94, v96, v97
	v_cvt_pk_bf16_f32 v95, v98, v99
	v_cvt_pk_bf16_f32 v96, v92, v93
	v_cvt_pk_bf16_f32 v97, v102, v103
	v_mad_i64_i32 v[92:93], s[0:1], v2, s55, v[172:173]
	flat_store_dwordx4 v[92:93], v[94:97]
	v_add_u32_e32 v2, 0x90, v166
	s_nop 0
	v_pk_mul_f32 v[94:95], v[86:87], v[132:133]
	v_cvt_pk_bf16_f32 v86, v88, v89
	v_cvt_pk_bf16_f32 v87, v90, v91
	v_cvt_pk_bf16_f32 v88, v84, v85
	v_cvt_pk_bf16_f32 v89, v94, v95
	v_mad_i64_i32 v[84:85], s[0:1], v2, s55, v[172:173]
	flat_store_dwordx4 v[84:85], v[86:89]
	v_add_u32_e32 v2, 0xa0, v166
	s_nop 0
	v_pk_mul_f32 v[86:87], v[78:79], v[132:133]
	v_pk_mul_f32 v[78:79], v[76:77], v[178:179]
	v_cvt_pk_bf16_f32 v76, v80, v81
	v_cvt_pk_bf16_f32 v77, v82, v83
	v_cvt_pk_bf16_f32 v78, v78, v79
	v_cvt_pk_bf16_f32 v79, v86, v87
	v_mad_i64_i32 v[86:87], s[0:1], v2, s55, v[172:173]
	flat_store_dwordx4 v[86:87], v[76:79]
	v_add_u32_e32 v2, 0xb0, v166
	v_mad_i64_i32 v[88:89], s[0:1], v2, s55, v[172:173]
	v_pk_mul_f32 v[76:77], v[70:71], v[132:133]
	v_pk_mul_f32 v[70:71], v[68:69], v[178:179]
	v_cvt_pk_bf16_f32 v68, v72, v73
	v_cvt_pk_bf16_f32 v69, v74, v75
	v_cvt_pk_bf16_f32 v70, v70, v71
	v_cvt_pk_bf16_f32 v71, v76, v77
	flat_store_dwordx4 v[88:89], v[68:71]
	v_or_b32_e32 v76, 0x81, v170
	v_ashrrev_i32_e32 v77, 31, v76
	v_or_b32_e32 v68, 0x80, v170
	v_ashrrev_i32_e32 v69, 31, v68
	v_lshlrev_b64 v[68:69], 6, v[68:69]
	v_lshlrev_b64 v[76:77], 6, v[76:77]
	v_lshl_add_u64 v[72:73], s[2:3], 0, v[68:69]
	v_lshl_add_u64 v[80:81], s[2:3], 0, v[76:77]
	flat_load_dwordx4 v[68:71], v[72:73] offset:32
	flat_load_dwordx4 v[236:239], v[72:73] offset:160
	flat_load_dwordx4 v[240:243], v[72:73] offset:176
	flat_load_dwordx4 v[244:247], v[72:73] offset:224
	flat_load_dwordx4 v[248:251], v[72:73] offset:240
	s_nop 0
	flat_load_dwordx4 v[72:75], v[72:73] offset:48
	s_nop 0
	flat_load_dwordx4 v[76:79], v[80:81] offset:32
	s_nop 0
	flat_load_dwordx4 v[80:83], v[80:81] offset:48
	s_waitcnt vmcnt(0) lgkmcnt(0)
	v_mov_b32_e32 v90, v68
	v_mov_b32_e32 v91, v76
	v_mov_b32_e32 v76, v69
	v_pk_add_f32 v[68:69], v[90:91], v[76:77]
	v_mov_b32_e32 v76, v70
	v_mov_b32_e32 v77, v78
	v_mov_b32_e32 v78, v71
	v_pk_add_f32 v[70:71], v[76:77], v[78:79]
	v_or_b32_e32 v76, 0x83, v170
	v_pk_add_f32 v[68:69], v[68:69], v[70:71]
	v_mov_b32_e32 v70, v72
	v_mov_b32_e32 v71, v80
	v_mov_b32_e32 v80, v73
	v_mov_b32_e32 v72, v74
	v_mov_b32_e32 v73, v82
	v_mov_b32_e32 v82, v75
	v_pk_add_f32 v[70:71], v[70:71], v[80:81]
	v_pk_add_f32 v[72:73], v[72:73], v[82:83]
	v_ashrrev_i32_e32 v77, 31, v76
	v_pk_add_f32 v[70:71], v[70:71], v[72:73]
	v_lshlrev_b64 v[76:77], 6, v[76:77]
	v_pk_add_f32 v[68:69], v[68:69], v[70:71]
	v_lshl_add_u64 v[80:81], s[2:3], 0, v[76:77]
	v_pk_fma_f32 v[68:69], v[68:69], s[6:7], v[168:169] op_sel_hi:[1,0,0]
	s_nop 0
	v_mul_f32_e32 v2, 0x4b800000, v68
	v_cmp_gt_f32_e64 s[4:5], s58, v68
	v_cmp_gt_f32_e32 vcc, s58, v69
	s_nop 0
	v_cndmask_b32_e64 v2, v68, v2, s[4:5]
	v_rsq_f32_e32 v68, v2
	v_mul_f32_e32 v2, 0x4b800000, v69
	v_cndmask_b32_e32 v2, v69, v2, vcc
	v_rsq_f32_e32 v69, v2
	s_nop 0
	v_pk_mul_f32 v[70:71], v[68:69], s[12:13] op_sel_hi:[1,0]
	s_nop 0
	v_cndmask_b32_e64 v90, v68, v70, s[4:5]
	v_or_b32_e32 v68, 0x82, v170
	v_cndmask_b32_e32 v91, v69, v71, vcc
	v_ashrrev_i32_e32 v69, 31, v68
	v_lshlrev_b64 v[68:69], 6, v[68:69]
	v_lshl_add_u64 v[72:73], s[2:3], 0, v[68:69]
	v_mov_b64_e32 v[68:69], v[236:237]
	v_mov_b64_e32 v[70:71], v[238:239]
	s_nop 0
	v_mov_b64_e32 v[72:73], v[240:241]
	v_mov_b64_e32 v[74:75], v[242:243]
	s_nop 0
	v_mov_b64_e32 v[76:77], v[244:245]
	v_mov_b64_e32 v[78:79], v[246:247]
	s_nop 0
	v_mov_b64_e32 v[80:81], v[248:249]
	v_mov_b64_e32 v[82:83], v[250:251]
	v_pk_mul_f32 v[64:65], v[64:65], v[90:91]
	v_pk_mul_f32 v[56:57], v[56:57], v[90:91]
	v_pk_mul_f32 v[48:49], v[48:49], v[90:91]
	v_pk_mul_f32 v[40:41], v[40:41], v[90:91]
	v_pk_mul_f32 v[32:33], v[32:33], v[90:91]
	v_pk_mul_f32 v[24:25], v[24:25], v[90:91]
	v_pk_mul_f32 v[16:17], v[16:17], v[90:91]
	v_pk_mul_f32 v[8:9], v[8:9], v[90:91]
	v_mov_b32_e32 v94, v68
	v_mov_b32_e32 v95, v76
	v_mov_b32_e32 v76, v69
	v_pk_add_f32 v[68:69], v[94:95], v[76:77]
	v_mov_b32_e32 v76, v70
	v_mov_b32_e32 v77, v78
	v_mov_b32_e32 v78, v71
	v_pk_add_f32 v[70:71], v[76:77], v[78:79]
	v_or_b32_e32 v76, 0x85, v170
	v_pk_add_f32 v[68:69], v[68:69], v[70:71]
	v_mov_b32_e32 v70, v72
	v_mov_b32_e32 v71, v80
	v_mov_b32_e32 v80, v73
	v_mov_b32_e32 v72, v74
	v_mov_b32_e32 v73, v82
	v_mov_b32_e32 v82, v75
	v_pk_add_f32 v[70:71], v[70:71], v[80:81]
	v_pk_add_f32 v[72:73], v[72:73], v[82:83]
	v_ashrrev_i32_e32 v77, 31, v76
	v_pk_add_f32 v[70:71], v[70:71], v[72:73]
	v_lshlrev_b64 v[76:77], 6, v[76:77]
	v_pk_add_f32 v[68:69], v[68:69], v[70:71]
	v_lshl_add_u64 v[80:81], s[2:3], 0, v[76:77]
	v_pk_fma_f32 v[68:69], v[68:69], s[6:7], v[168:169] op_sel_hi:[1,0,0]
	s_nop 0
	v_mul_f32_e32 v2, 0x4b800000, v68
	v_cmp_gt_f32_e64 s[4:5], s58, v68
	v_cmp_gt_f32_e32 vcc, s58, v69
	s_nop 0
	v_cndmask_b32_e64 v2, v68, v2, s[4:5]
	v_rsq_f32_e32 v68, v2
	v_mul_f32_e32 v2, 0x4b800000, v69
	v_cndmask_b32_e32 v2, v69, v2, vcc
	v_rsq_f32_e32 v69, v2
	s_nop 0
	v_pk_mul_f32 v[70:71], v[68:69], s[12:13] op_sel_hi:[1,0]
	s_nop 0
	v_cndmask_b32_e64 v94, v68, v70, s[4:5]
	v_or_b32_e32 v68, 0x84, v170
	v_cndmask_b32_e32 v95, v69, v71, vcc
	v_ashrrev_i32_e32 v69, 31, v68
	v_lshlrev_b64 v[68:69], 6, v[68:69]
	v_lshl_add_u64 v[72:73], s[2:3], 0, v[68:69]
	flat_load_dwordx4 v[68:71], v[72:73] offset:32
	flat_load_dwordx4 v[236:239], v[72:73] offset:160
	flat_load_dwordx4 v[240:243], v[72:73] offset:176
	flat_load_dwordx4 v[244:247], v[72:73] offset:224
	flat_load_dwordx4 v[248:251], v[72:73] offset:240
	s_nop 0
	flat_load_dwordx4 v[72:75], v[72:73] offset:48
	s_nop 0
	flat_load_dwordx4 v[76:79], v[80:81] offset:32
	s_nop 0
	flat_load_dwordx4 v[80:83], v[80:81] offset:48
	v_pk_mul_f32 v[66:67], v[66:67], v[94:95]
	v_pk_mul_f32 v[58:59], v[58:59], v[94:95]
	v_pk_mul_f32 v[50:51], v[50:51], v[94:95]
	v_pk_mul_f32 v[42:43], v[42:43], v[94:95]
	v_pk_mul_f32 v[34:35], v[34:35], v[94:95]
	v_pk_mul_f32 v[26:27], v[26:27], v[94:95]
	v_pk_mul_f32 v[18:19], v[18:19], v[94:95]
	v_pk_mul_f32 v[10:11], v[10:11], v[94:95]
	s_waitcnt vmcnt(0) lgkmcnt(0)
	v_mov_b32_e32 v96, v68
	v_mov_b32_e32 v97, v76
	v_mov_b32_e32 v76, v69
	v_pk_add_f32 v[68:69], v[96:97], v[76:77]
	v_mov_b32_e32 v76, v70
	v_mov_b32_e32 v77, v78
	v_mov_b32_e32 v78, v71
	v_pk_add_f32 v[70:71], v[76:77], v[78:79]
	v_or_b32_e32 v76, 0x87, v170
	v_pk_add_f32 v[68:69], v[68:69], v[70:71]
	v_mov_b32_e32 v70, v72
	v_mov_b32_e32 v71, v80
	v_mov_b32_e32 v80, v73
	v_mov_b32_e32 v72, v74
	v_mov_b32_e32 v73, v82
	v_mov_b32_e32 v82, v75
	v_pk_add_f32 v[70:71], v[70:71], v[80:81]
	v_pk_add_f32 v[72:73], v[72:73], v[82:83]
	v_ashrrev_i32_e32 v77, 31, v76
	v_pk_add_f32 v[70:71], v[70:71], v[72:73]
	v_lshlrev_b64 v[76:77], 6, v[76:77]
	v_pk_add_f32 v[68:69], v[68:69], v[70:71]
	v_lshl_add_u64 v[80:81], s[2:3], 0, v[76:77]
	v_pk_fma_f32 v[68:69], v[68:69], s[6:7], v[168:169] op_sel_hi:[1,0,0]
	s_nop 0
	v_mul_f32_e32 v2, 0x4b800000, v68
	v_cmp_gt_f32_e64 s[4:5], s58, v68
	v_cmp_gt_f32_e32 vcc, s58, v69
	s_nop 0
	v_cndmask_b32_e64 v2, v68, v2, s[4:5]
	v_rsq_f32_e32 v68, v2
	v_mul_f32_e32 v2, 0x4b800000, v69
	v_cndmask_b32_e32 v2, v69, v2, vcc
	v_rsq_f32_e32 v69, v2
	s_nop 0
	v_pk_mul_f32 v[70:71], v[68:69], s[12:13] op_sel_hi:[1,0]
	s_nop 0
	v_cndmask_b32_e64 v96, v68, v70, s[4:5]
	v_or_b32_e32 v68, 0x86, v170
	v_cndmask_b32_e32 v97, v69, v71, vcc
	v_ashrrev_i32_e32 v69, 31, v68
	v_lshlrev_b64 v[68:69], 6, v[68:69]
	v_lshl_add_u64 v[68:69], s[2:3], 0, v[68:69]
	v_mov_b64_e32 v[72:73], v[236:237]
	v_mov_b64_e32 v[74:75], v[238:239]
	s_nop 0
	v_mov_b64_e32 v[68:69], v[240:241]
	v_mov_b64_e32 v[70:71], v[242:243]
	s_nop 0
	v_mov_b64_e32 v[76:77], v[244:245]
	v_mov_b64_e32 v[78:79], v[246:247]
	s_nop 0
	v_mov_b64_e32 v[80:81], v[248:249]
	v_mov_b64_e32 v[82:83], v[250:251]
	v_mov_b32_e32 v98, v72
	v_mov_b32_e32 v99, v76
	v_mov_b32_e32 v76, v73
	v_pk_add_f32 v[72:73], v[98:99], v[76:77]
	v_mov_b32_e32 v76, v74
	v_mov_b32_e32 v77, v78
	v_mov_b32_e32 v78, v75
	v_pk_add_f32 v[74:75], v[76:77], v[78:79]
	s_nop 0
	v_pk_add_f32 v[72:73], v[72:73], v[74:75]
	v_mov_b32_e32 v74, v68
	v_mov_b32_e32 v75, v80
	v_mov_b32_e32 v80, v69
	v_pk_add_f32 v[68:69], v[74:75], v[80:81]
	v_mov_b32_e32 v74, v70
	v_mov_b32_e32 v75, v82
	v_mov_b32_e32 v82, v71
	v_pk_add_f32 v[70:71], v[74:75], v[82:83]
	s_nop 0
	v_pk_add_f32 v[68:69], v[68:69], v[70:71]
	s_nop 0
	v_pk_add_f32 v[68:69], v[72:73], v[68:69]
	s_nop 0
	v_pk_fma_f32 v[68:69], v[68:69], s[6:7], v[168:169] op_sel_hi:[1,0,0]
	s_nop 0
	v_mul_f32_e32 v2, 0x4b800000, v68
	v_cmp_gt_f32_e64 s[4:5], s58, v68
	v_cmp_gt_f32_e32 vcc, s58, v69
	s_nop 0
	v_cndmask_b32_e64 v2, v68, v2, s[4:5]
	v_rsq_f32_e32 v68, v2
	v_mul_f32_e32 v2, 0x4b800000, v69
	v_cndmask_b32_e32 v2, v69, v2, vcc
	v_rsq_f32_e32 v69, v2
	s_nop 0
	v_pk_mul_f32 v[70:71], v[68:69], s[12:13] op_sel_hi:[1,0]
	s_nop 0
	v_cndmask_b32_e32 v69, v69, v71, vcc
	v_cndmask_b32_e64 v68, v68, v70, s[4:5]
	v_pk_mul_f32 v[70:71], v[62:63], v[68:69]
	v_pk_mul_f32 v[62:63], v[60:61], v[96:97]
	v_cvt_pk_bf16_f32 v60, v64, v65
	v_cvt_pk_bf16_f32 v61, v66, v67
	v_cvt_pk_bf16_f32 v62, v62, v63
	v_cvt_pk_bf16_f32 v63, v70, v71
	flat_store_dwordx4 v[124:125], v[60:63] offset:256
	s_nop 1
	v_pk_mul_f32 v[60:61], v[54:55], v[68:69]
	v_pk_mul_f32 v[54:55], v[52:53], v[96:97]
	v_cvt_pk_bf16_f32 v52, v56, v57
	v_cvt_pk_bf16_f32 v53, v58, v59
	v_cvt_pk_bf16_f32 v54, v54, v55
	v_cvt_pk_bf16_f32 v55, v60, v61
	flat_store_dwordx4 v[116:117], v[52:55] offset:256
	s_nop 1
	v_pk_mul_f32 v[52:53], v[46:47], v[68:69]
	v_pk_mul_f32 v[46:47], v[44:45], v[96:97]
	v_cvt_pk_bf16_f32 v44, v48, v49
	v_cvt_pk_bf16_f32 v45, v50, v51
	v_cvt_pk_bf16_f32 v46, v46, v47
	v_cvt_pk_bf16_f32 v47, v52, v53
	flat_store_dwordx4 v[108:109], v[44:47] offset:256
	s_nop 1
	v_pk_mul_f32 v[44:45], v[38:39], v[68:69]
	v_pk_mul_f32 v[38:39], v[36:37], v[96:97]
	v_cvt_pk_bf16_f32 v36, v40, v41
	v_cvt_pk_bf16_f32 v37, v42, v43
	v_cvt_pk_bf16_f32 v38, v38, v39
	v_cvt_pk_bf16_f32 v39, v44, v45
	flat_store_dwordx4 v[100:101], v[36:39] offset:256
	s_nop 1
	v_pk_mul_f32 v[36:37], v[30:31], v[68:69]
	v_pk_mul_f32 v[30:31], v[28:29], v[96:97]
	v_cvt_pk_bf16_f32 v28, v32, v33
	v_cvt_pk_bf16_f32 v29, v34, v35
	v_cvt_pk_bf16_f32 v30, v30, v31
	v_cvt_pk_bf16_f32 v31, v36, v37
	flat_store_dwordx4 v[92:93], v[28:31] offset:256
	s_nop 1
	v_pk_mul_f32 v[28:29], v[22:23], v[68:69]
	v_pk_mul_f32 v[22:23], v[20:21], v[96:97]
	v_cvt_pk_bf16_f32 v20, v24, v25
	v_cvt_pk_bf16_f32 v21, v26, v27
	v_cvt_pk_bf16_f32 v22, v22, v23
	v_cvt_pk_bf16_f32 v23, v28, v29
	flat_store_dwordx4 v[84:85], v[20:23] offset:256
	s_nop 1
	v_pk_mul_f32 v[20:21], v[14:15], v[68:69]
	v_pk_mul_f32 v[14:15], v[12:13], v[96:97]
	v_cvt_pk_bf16_f32 v12, v16, v17
	v_cvt_pk_bf16_f32 v13, v18, v19
	v_cvt_pk_bf16_f32 v14, v14, v15
	v_cvt_pk_bf16_f32 v15, v20, v21
	flat_store_dwordx4 v[86:87], v[12:15] offset:256
	s_nop 1
	v_pk_mul_f32 v[12:13], v[6:7], v[68:69]
	v_pk_mul_f32 v[6:7], v[4:5], v[96:97]
	v_cvt_pk_bf16_f32 v4, v8, v9
	v_cvt_pk_bf16_f32 v5, v10, v11
	v_cvt_pk_bf16_f32 v6, v6, v7
	v_cvt_pk_bf16_f32 v7, v12, v13
	flat_store_dwordx4 v[88:89], v[4:7] offset:256
	s_andn2_b64 vcc, exec, s[26:27]
	s_mov_b64 s[4:5], -1
	s_cbranch_vccnz .LBB6_759
